# masked attention softmax: mask applied with v_bfe_i32+v_bfi_b32 (bfe fills the MFMA shadow, no VCC nops), bpermute lane address hoisted out of the tile loop
# speedup vs baseline: 1.0015x; 1.0015x over previous
.LBB0_1633:
	s_or_b64 exec, exec, s[4:5]
	v_mov_b32_e32 v16, v3
	v_mov_b32_e32 v17, v3
	v_mov_b32_e32 v2, v3
	v_mov_b32_e32 v4, v3
	v_mov_b32_e32 v5, v3
	v_mov_b32_e32 v6, v3
	v_mov_b32_e32 v7, v3
	v_mov_b32_e32 v8, v3
	v_mov_b32_e32 v9, v3
	v_mov_b32_e32 v10, v3
	v_mov_b32_e32 v11, v3
	v_mov_b32_e32 v12, v3
	v_mov_b32_e32 v13, v3
	v_mov_b32_e32 v14, v3
	v_mov_b32_e32 v15, v3
	v_mov_b64_e32 v[34:35], v[16:17]
	v_mov_b64_e32 v[32:33], v[14:15]
	v_mov_b64_e32 v[30:31], v[12:13]
	v_mov_b64_e32 v[28:29], v[10:11]
	v_mov_b64_e32 v[26:27], v[8:9]
	v_mov_b64_e32 v[24:25], v[6:7]
	v_mov_b64_e32 v[22:23], v[4:5]
	v_mov_b64_e32 v[20:21], v[2:3]
	v_mov_b64_e32 v[18:19], v[16:17]
	s_mov_b32 s16, 0
	v_mov_b32_e32 v90, 0xf149f2ca
	v_mov_b32_e32 v110, 0
	s_movk_i32 s50, 0xa0
	s_mov_b64 s[4:5], 0
	v_mov_b64_e32 v[88:89], v[82:83]
	v_mov_b32_e32 v111, v109
	v_mov_b32_e32 v112, v101
	v_mov_b32_e32 v113, v69
	v_mov_b64_e32 v[16:17], v[14:15]
	v_mov_b64_e32 v[14:15], v[12:13]
	v_mov_b64_e32 v[12:13], v[10:11]
	v_mov_b64_e32 v[10:11], v[8:9]
	v_mov_b64_e32 v[8:9], v[6:7]
	v_mov_b64_e32 v[6:7], v[4:5]
	v_mov_b64_e32 v[4:5], v[2:3]
	s_mov_b32 s17, 0
	v_and_b32_e32 v195, 64, v214
	v_xor_b32_e32 v194, 32, v214
	v_add_u32_e32 v195, 64, v195
	v_cmp_lt_i32_e32 vcc, v194, v195
	s_nop 1
	v_cndmask_b32_e32 v194, v214, v194, vcc
	v_lshlrev_b32_e32 v194, 2, v194
	s_waitcnt vmcnt(0) lgkmcnt(0)
	s_barrier
	s_branch .LBB0_1636

.LBB0_1654:
	s_or_b64 exec, exec, s[8:9]
	v_cmp_le_u32_e32 vcc, s17, v97
	s_and_saveexec_b64 s[8:9], vcc
	s_cbranch_execz .LBB0_1635
	s_lshl_b32 s10, s16, 14
	s_setprio 1
	v_add3_u32 v2, s10, v93, v92
	v_add3_u32 v174, s10, v94, v92
	v_add3_u32 v175, s10, v95, v92
	v_add3_u32 v176, s10, v96, v92
	ds_read_b128 v[36:39], v2 offset:50048
	ds_read_b128 v[114:117], v174 offset:50048
	ds_read_b128 v[132:135], v175 offset:50048
	ds_read_b128 v[136:139], v176 offset:50048
	ds_read_b32 v177, v112
	ds_read2_b32 v[140:141], v113 offset0:26 offset1:27
	ds_read2_b32 v[142:143], v113 offset0:24 offset1:25
	ds_read2_b32 v[144:145], v113 offset0:18 offset1:19
	ds_read2_b32 v[146:147], v113 offset0:16 offset1:17
	ds_read2_b32 v[148:149], v113 offset0:10 offset1:11
	ds_read2_b32 v[150:151], v113 offset0:8 offset1:9
	ds_read2_b32 v[152:153], v113 offset0:2 offset1:3
	ds_read2_b32 v[154:155], v113 offset1:1
	s_waitcnt lgkmcnt(12)
	v_mfma_f32_32x32x16_bf16 v[36:51], v[36:39], v[52:55], 0
	s_waitcnt lgkmcnt(11)
	v_mfma_f32_32x32x16_bf16 v[36:51], v[114:117], v[56:59], v[36:51]
	s_waitcnt lgkmcnt(10)
	v_mfma_f32_32x32x16_bf16 v[36:51], v[132:135], v[60:63], v[36:51]
	s_waitcnt lgkmcnt(9)
	v_mfma_f32_32x32x16_bf16 v[36:51], v[136:139], v[64:67], v[36:51]
	s_setprio 0
	v_add3_u32 v174, s10, v98, v107
	v_add3_u32 v175, s10, v99, v107
	ds_read_b128 v[156:159], v174 offset:58240
	ds_read_b128 v[162:165], v174 offset:60288
	ds_read_b128 v[166:169], v175 offset:58240
	ds_read_b128 v[170:173], v175 offset:60288
	s_waitcnt lgkmcnt(4)
	v_lshrrev_b32_e32 v2, v102, v177
	v_bfe_i32 v178, v2, 0, 1
	v_bfe_i32 v179, v2, 1, 1
	v_bfe_i32 v180, v2, 2, 1
	v_bfe_i32 v181, v2, 3, 1
	v_bfe_i32 v182, v2, 8, 1
	v_bfe_i32 v183, v2, 9, 1
	v_bfe_i32 v184, v2, 10, 1
	v_bfe_i32 v185, v2, 11, 1
	v_bfe_i32 v186, v2, 16, 1
	v_bfe_i32 v187, v2, 17, 1
	v_bfe_i32 v188, v2, 18, 1
	v_bfe_i32 v189, v2, 19, 1
	v_bfe_i32 v190, v2, 24, 1
	v_bfe_i32 v191, v2, 25, 1
	v_bfe_i32 v192, v2, 26, 1
	v_bfe_i32 v193, v2, 27, 1
	v_pk_fma_f32 v[36:37], v[36:37], s[82:83], v[140:141] op_sel:[0,0,1] op_sel_hi:[1,0,0]
	v_pk_fma_f32 v[38:39], v[38:39], s[82:83], v[142:143] op_sel:[0,0,1] op_sel_hi:[1,0,0]
	v_bfi_b32 v36, v178, v36, v228
	v_bfi_b32 v37, v179, v37, v228
	v_bfi_b32 v38, v180, v38, v228
	v_bfi_b32 v39, v181, v39, v228
	v_max_f32_e32 v116, v36, v37
	v_max_f32_e32 v114, v38, v39
	v_max3_f32 v116, v116, s90, v114
	v_pk_fma_f32 v[40:41], v[40:41], s[82:83], v[144:145] op_sel:[0,0,1] op_sel_hi:[1,0,0]
	v_pk_fma_f32 v[42:43], v[42:43], s[82:83], v[146:147] op_sel:[0,0,1] op_sel_hi:[1,0,0]
	v_bfi_b32 v40, v182, v40, v228
	v_bfi_b32 v41, v183, v41, v228
	v_bfi_b32 v42, v184, v42, v228
	v_bfi_b32 v43, v185, v43, v228
	v_max_f32_e32 v117, v40, v41
	v_max_f32_e32 v114, v42, v43
	v_max3_f32 v116, v116, v117, v114
	v_pk_fma_f32 v[44:45], v[44:45], s[82:83], v[148:149] op_sel:[0,0,1] op_sel_hi:[1,0,0]
	v_pk_fma_f32 v[46:47], v[46:47], s[82:83], v[150:151] op_sel:[0,0,1] op_sel_hi:[1,0,0]
	v_bfi_b32 v44, v186, v44, v228
	v_bfi_b32 v45, v187, v45, v228
	v_bfi_b32 v46, v188, v46, v228
	v_bfi_b32 v47, v189, v47, v228
	v_max_f32_e32 v117, v44, v45
	v_max_f32_e32 v114, v46, v47
	v_max3_f32 v116, v116, v117, v114
	v_pk_fma_f32 v[48:49], v[48:49], s[82:83], v[152:153] op_sel:[0,0,1] op_sel_hi:[1,0,0]
	v_pk_fma_f32 v[50:51], v[50:51], s[82:83], v[154:155] op_sel:[0,0,1] op_sel_hi:[1,0,0]
	v_bfi_b32 v48, v190, v48, v228
	v_bfi_b32 v49, v191, v49, v228
	v_bfi_b32 v50, v192, v50, v228
	v_bfi_b32 v51, v193, v51, v228
	v_max_f32_e32 v117, v48, v49
	v_max_f32_e32 v2, v50, v51
	v_max3_f32 v2, v116, v117, v2
	ds_bpermute_b32 v114, v194, v2
	s_waitcnt lgkmcnt(0)
	v_max_f32_e32 v114, v114, v114
	v_max_f32_e32 v2, v2, v114
	v_add_f32_e32 v114, 0x41000000, v90
	v_cmp_gt_f32_e32 vcc, v2, v114
	s_cbranch_vccz .LBB0_1634
	v_max_f32_e32 v2, v2, v2
	v_max_f32_e32 v114, v90, v90
	v_max_f32_e32 v114, v114, v2
	v_sub_f32_e32 v2, v90, v114
	v_exp_f32_e32 v2, v2
	v_mov_b32_e32 v90, v114
	v_pk_mul_f32 v[34:35], v[34:35], v[2:3] op_sel_hi:[1,0]
	v_pk_mul_f32 v[32:33], v[32:33], v[2:3] op_sel_hi:[1,0]
	v_pk_mul_f32 v[30:31], v[30:31], v[2:3] op_sel_hi:[1,0]
	v_pk_mul_f32 v[28:29], v[28:29], v[2:3] op_sel_hi:[1,0]
	v_pk_mul_f32 v[26:27], v[26:27], v[2:3] op_sel_hi:[1,0]
	v_pk_mul_f32 v[24:25], v[24:25], v[2:3] op_sel_hi:[1,0]
	v_pk_mul_f32 v[22:23], v[22:23], v[2:3] op_sel_hi:[1,0]
	v_pk_mul_f32 v[20:21], v[20:21], v[2:3] op_sel_hi:[1,0]
	v_pk_mul_f32 v[18:19], v[18:19], v[2:3] op_sel_hi:[1,0]
	v_pk_mul_f32 v[16:17], v[16:17], v[2:3] op_sel_hi:[1,0]
	v_pk_mul_f32 v[14:15], v[14:15], v[2:3] op_sel_hi:[1,0]
	v_pk_mul_f32 v[12:13], v[12:13], v[2:3] op_sel_hi:[1,0]
	v_pk_mul_f32 v[10:11], v[10:11], v[2:3] op_sel_hi:[1,0]
	v_pk_mul_f32 v[8:9], v[8:9], v[2:3] op_sel_hi:[1,0]
	v_pk_mul_f32 v[6:7], v[6:7], v[2:3] op_sel_hi:[1,0]
	v_pk_mul_f32 v[4:5], v[4:5], v[2:3] op_sel_hi:[1,0]
	v_mul_f32_e32 v110, v110, v2
	s_branch .LBB0_1634
